# grid barrier: acquire invalidate issued before polling (followers) and together with the L2 write-back (leaders) so its latency overlaps the wait
# speedup vs baseline: 1.0211x; 1.0079x over previous
.LBB0_158:
	s_or_b64 exec, exec, s[2:3]
	v_mov_b32_e32 v1, s25
	v_add_co_u32_e32 v4, vcc, 0x2000, v1
	v_mov_b32_e32 v1, s24
	s_nop 0
	v_addc_co_u32_e32 v5, vcc, 0, v1, vcc
	s_waitcnt vmcnt(0) lgkmcnt(0)
	s_waitcnt vmcnt(0)

.LBB0_193:
	v_readlane_b32 s4, v251, 48
	s_lshl_b32 s4, s4, 2
	s_add_u32 s25, s2, s4
	s_addc_u32 s24, s3, 0
	v_mov_b32_e32 v1, s25
	v_add_co_u32_e32 v8, vcc, 0x1000, v1
	v_mov_b32_e32 v1, s24
	s_nop 0
	v_addc_co_u32_e32 v9, vcc, 0, v1, vcc
	flat_atomic_add v1, v[8:9], v211 offset:1024 sc0
	v_cvt_f32_u32_e32 v3, v6
	v_sub_u32_e32 v5, 0, v6
	v_rcp_iflag_f32_e32 v3, v3
	s_nop 0
	v_mul_f32_e32 v3, 0x4f7ffffe, v3
	v_cvt_u32_f32_e32 v3, v3
	v_mul_lo_u32 v5, v5, v3
	v_mul_hi_u32 v5, v3, v5
	v_add_u32_e32 v3, v3, v5
	s_waitcnt vmcnt(0) lgkmcnt(0)
	v_mul_hi_u32 v3, v1, v3
	v_mul_lo_u32 v7, v3, v6
	v_add_u32_e32 v5, 1, v1
	v_sub_u32_e32 v1, v1, v7
	v_add_u32_e32 v8, 1, v3
	v_cmp_ge_u32_e32 vcc, v1, v6
	v_sub_u32_e32 v7, v1, v6
	s_nop 0
	v_cndmask_b32_e32 v3, v3, v8, vcc
	v_cndmask_b32_e32 v1, v1, v7, vcc
	v_add_u32_e32 v7, 1, v3
	v_cmp_ge_u32_e32 vcc, v1, v6
	s_nop 1
	v_cndmask_b32_e32 v1, v3, v7, vcc
	v_mad_u64_u32 v[6:7], s[4:5], v6, v1, v[6:7]
	v_cmp_ne_u32_e32 vcc, v5, v6
	s_and_saveexec_b64 s[4:5], vcc
	s_xor_b64 s[4:5], exec, s[4:5]
	s_cbranch_execz .LBB0_206
	v_mad_u32_u24 v255, v4, v1, 1
	buffer_inv sc1
	v_mov_b32_e32 v3, s25
	v_add_co_u32_e32 v4, vcc, 0x2000, v3
	v_mov_b32_e32 v3, s24
	s_nop 0
	v_addc_co_u32_e32 v5, vcc, 0, v3, vcc
	flat_load_dword v3, v[4:5] offset:1024 sc1
	s_add_u32 s8, s25, 0x2400
	s_addc_u32 s9, s24, 0
	s_waitcnt vmcnt(0) lgkmcnt(0)
	v_cmp_lt_u32_e32 vcc, v3, v255
	s_and_saveexec_b64 s[6:7], vcc
	s_cbranch_execz .LBB0_205
	s_mov_b32 s26, 1
	s_mov_b64 s[10:11], 0
	s_branch .LBB0_197

.LBB0_205:
	s_or_b64 exec, exec, s[6:7]
	s_waitcnt vmcnt(0) lgkmcnt(0)
	s_waitcnt vmcnt(0)
.LBB0_206:
	s_andn2_saveexec_b64 s[4:5], s[4:5]
	s_cbranch_execz .LBB0_222
	v_mad_u32_u24 v255, v4, v1, 1
	buffer_wbl2 sc1
	buffer_inv sc1
	s_waitcnt vmcnt(0)
	s_add_u32 s4, s2, 0x2400
	s_addc_u32 s5, s3, 0
	v_mov_b64_e32 v[4:5], s[4:5]
	flat_atomic_add v[4:5], v211
	flat_atomic_add v[4:5], v211 offset:256
	flat_atomic_add v[4:5], v211 offset:512
	flat_atomic_add v[4:5], v211 offset:768
	flat_atomic_add v[4:5], v211 offset:1024
	flat_atomic_add v[4:5], v211 offset:1280
	flat_atomic_add v[4:5], v211 offset:1536
	flat_atomic_add v[4:5], v211 offset:1792
	flat_atomic_add v[4:5], v211 offset:2048
	flat_atomic_add v[4:5], v211 offset:2304
	flat_atomic_add v[4:5], v211 offset:2560
	flat_atomic_add v[4:5], v211 offset:2816
	flat_atomic_add v[4:5], v211 offset:3072
	flat_atomic_add v[4:5], v211 offset:3328
	flat_atomic_add v[4:5], v211 offset:3584
	flat_atomic_add v[4:5], v211 offset:3840
	s_add_u32 s4, s25, 0x2400
	s_addc_u32 s5, s24, 0
	s_mov_b64 s[8:9], 0
	v_cmp_eq_u32_e32 vcc, v255, v255
	v_mov_b64_e32 v[4:5], s[4:5]
	s_and_saveexec_b64 s[6:7], vcc
	s_cbranch_execz .LBB0_219
	v_mov_b64_e32 v[4:5], s[4:5]
	flat_load_dword v3, v[4:5] sc1
	s_mov_b64 s[12:13], 0
	s_waitcnt vmcnt(0) lgkmcnt(0)
	v_cmp_lt_u32_e32 vcc, v3, v255
	s_and_saveexec_b64 s[10:11], vcc
	s_cbranch_execz .LBB0_218
	s_add_u32 s8, s2, 0x200
	s_addc_u32 s9, s3, 0
	s_mov_b32 s22, 1
	s_mov_b64 s[2:3], 0
	s_branch .LBB0_211

.LBB0_360:
	v_readlane_b32 s4, v251, 48
	s_lshl_b32 s4, s4, 2
	s_add_u32 s25, s2, s4
	s_addc_u32 s24, s3, 0
	v_mov_b32_e32 v1, s25
	v_add_co_u32_e32 v8, vcc, 0x1000, v1
	v_mov_b32_e32 v1, s24
	s_nop 0
	v_addc_co_u32_e32 v9, vcc, 0, v1, vcc
	flat_atomic_add v3, v[8:9], v211 offset:1024 sc0
	v_cvt_f32_u32_e32 v1, v6
	v_sub_u32_e32 v5, 0, v6
	v_rcp_iflag_f32_e32 v1, v1
	s_nop 0
	v_mul_f32_e32 v1, 0x4f7ffffe, v1
	v_cvt_u32_f32_e32 v1, v1
	v_mul_lo_u32 v5, v5, v1
	v_mul_hi_u32 v5, v1, v5
	v_add_u32_e32 v1, v1, v5
	s_waitcnt vmcnt(0) lgkmcnt(0)
	v_mul_hi_u32 v1, v3, v1
	v_mul_lo_u32 v5, v1, v6
	v_sub_u32_e32 v5, v3, v5
	v_cmp_ge_u32_e32 vcc, v5, v6
	v_add_u32_e32 v7, 1, v1
	v_add_u32_e32 v3, 1, v3
	v_cndmask_b32_e32 v1, v1, v7, vcc
	v_sub_u32_e32 v7, v5, v6
	v_cndmask_b32_e32 v5, v5, v7, vcc
	v_cmp_ge_u32_e32 vcc, v5, v6
	v_add_u32_e32 v5, 1, v1
	s_nop 0
	v_cndmask_b32_e32 v1, v1, v5, vcc
	v_mad_u64_u32 v[6:7], s[4:5], v6, v1, v[6:7]
	v_cmp_ne_u32_e32 vcc, v3, v6
	s_and_saveexec_b64 s[4:5], vcc
	s_xor_b64 s[4:5], exec, s[4:5]
	s_cbranch_execz .LBB0_373
	v_mad_u32_u24 v255, v4, v1, 1
	buffer_inv sc1
	v_mov_b32_e32 v3, s25
	v_add_co_u32_e32 v4, vcc, 0x2000, v3
	v_mov_b32_e32 v3, s24
	s_nop 0
	v_addc_co_u32_e32 v5, vcc, 0, v3, vcc
	flat_load_dword v3, v[4:5] offset:1024 sc1
	s_add_u32 s8, s25, 0x2400
	s_addc_u32 s9, s24, 0
	s_waitcnt vmcnt(0) lgkmcnt(0)
	v_cmp_lt_u32_e32 vcc, v3, v255
	s_and_saveexec_b64 s[6:7], vcc
	s_cbranch_execz .LBB0_372
	s_mov_b32 s26, 1
	s_mov_b64 s[10:11], 0
	s_branch .LBB0_364

.LBB0_1326:
	v_mad_u32_u24 v255, v4, v1, 1
	buffer_wbl2 sc1
	buffer_inv sc1
	s_waitcnt vmcnt(0)
	s_add_u32 s4, s2, 0x2400
	s_addc_u32 s5, s3, 0
	v_mov_b64_e32 v[4:5], s[4:5]
	flat_atomic_add v[4:5], v211
	flat_atomic_add v[4:5], v211 offset:256
	flat_atomic_add v[4:5], v211 offset:512
	flat_atomic_add v[4:5], v211 offset:768
	flat_atomic_add v[4:5], v211 offset:1024
	flat_atomic_add v[4:5], v211 offset:1280
	flat_atomic_add v[4:5], v211 offset:1536
	flat_atomic_add v[4:5], v211 offset:1792
	flat_atomic_add v[4:5], v211 offset:2048
	flat_atomic_add v[4:5], v211 offset:2304
	flat_atomic_add v[4:5], v211 offset:2560
	flat_atomic_add v[4:5], v211 offset:2816
	flat_atomic_add v[4:5], v211 offset:3072
	flat_atomic_add v[4:5], v211 offset:3328
	flat_atomic_add v[4:5], v211 offset:3584
	flat_atomic_add v[4:5], v211 offset:3840
	s_add_u32 s4, s25, 0x2400
	s_addc_u32 s5, s24, 0
	s_mov_b64 s[8:9], 0
	v_cmp_eq_u32_e32 vcc, v255, v255
	v_mov_b64_e32 v[4:5], s[4:5]
	s_and_saveexec_b64 s[6:7], vcc
	s_cbranch_execz .LBB0_1338
	v_mov_b64_e32 v[4:5], s[4:5]
	flat_load_dword v3, v[4:5] sc1
	s_mov_b64 s[12:13], 0
	s_waitcnt vmcnt(0) lgkmcnt(0)
	v_cmp_lt_u32_e32 vcc, v3, v255
	s_and_saveexec_b64 s[10:11], vcc
	s_cbranch_execz .LBB0_1337
	s_add_u32 s8, s2, 0x200
	s_addc_u32 s9, s3, 0
	s_mov_b32 s22, 1
	s_mov_b64 s[2:3], 0
	s_branch .LBB0_1330
